# weight-conversion loops: converted rows written with the non-temporal store policy
# baseline (speedup 1.0000x reference)
.LBB0_91:
	s_waitcnt lgkmcnt(0)
	s_barrier
	s_waitcnt vmcnt(0)
	v_add_u32_e32 v6, s17, v74
	v_add_u32_e32 v3, s17, v76
	s_mov_b64 s[34:35], -1
	s_and_b64 vcc, exec, s[30:31]
	v_add_u32_e32 v2, v75, v68
	v_ashrrev_i32_e32 v8, 31, v6
	v_mul_lo_u32 v7, s19, v6
	v_ashrrev_i32_e32 v5, 31, v3
	v_mul_lo_u32 v4, s19, v3
	s_cbranch_vccz .LBB0_93
	ds_read2_b32 v[10:11], v2 offset1:1
	v_mov_b64_e32 v[12:13], s[10:11]
	v_mul_lo_u32 v9, s18, v8
	v_mad_u64_u32 v[14:15], s[30:31], s18, v6, v[12:13]
	v_add3_u32 v15, v7, v15, v9
	s_ashr_i32 s17, s16, 31
	v_lshl_add_u64 v[14:15], v[14:15], 0, s[16:17]
	v_add_u32_e32 v9, 0x1100, v2
	v_add_u32_e32 v18, 0x2200, v2
	v_add_u32_e32 v20, 0x3300, v2
	v_lshl_add_u64 v[14:15], v[14:15], 0, v[68:69]
	ds_read2_b32 v[16:17], v9 offset1:1
	ds_read2_b32 v[18:19], v18 offset1:1
	ds_read2_b32 v[20:21], v20 offset1:1
	s_waitcnt lgkmcnt(3)
	global_store_dwordx2 v[14:15], v[10:11], off nt
	v_mul_lo_u32 v9, s18, v5
	v_mad_u64_u32 v[10:11], s[30:31], s18, v3, v[12:13]
	v_add3_u32 v11, v4, v11, v9
	v_lshl_add_u64 v[10:11], v[10:11], 0, s[16:17]
	v_lshl_add_u64 v[10:11], v[10:11], 0, v[68:69]
	s_waitcnt lgkmcnt(2)
	global_store_dwordx2 v[10:11], v[16:17], off nt
	s_waitcnt lgkmcnt(1)
	global_store_dwordx2 v[14:15], v[18:19], off offset:64 nt
	s_waitcnt lgkmcnt(0)
	global_store_dwordx2 v[10:11], v[20:21], off offset:64 nt
	s_mov_b64 s[34:35], 0
.LBB0_93:
	s_andn2_b64 vcc, exec, s[34:35]
	v_lshlrev_b32_e32 v66, 1, v70
	s_cbranch_vccnz .LBB0_95
	ds_read2_b32 v[10:11], v77 offset1:1
	ds_read2_b32 v[12:13], v77 offset0:2 offset1:3
	v_mul_lo_u32 v14, s18, v8
	v_mad_u64_u32 v[8:9], s[30:31], s18, v6, 0
	v_add3_u32 v9, v9, v14, v7
	s_ashr_i32 s17, s16, 31
	v_lshl_add_u64 v[6:7], v[8:9], 1, s[10:11]
	s_lshl_b64 s[16:17], s[16:17], 1
	v_lshl_add_u64 v[6:7], v[6:7], 0, s[16:17]
	v_lshl_add_u64 v[18:19], v[6:7], 0, v[66:67]
	v_add_u32_e32 v6, 0x2100, v77
	v_add_u32_e32 v8, 0x2108, v77
	ds_read2_b32 v[6:7], v6 offset1:1
	ds_read2_b32 v[8:9], v8 offset1:1
	s_waitcnt lgkmcnt(2)
	global_store_dwordx4 v[18:19], v[10:13], off nt
	v_mul_lo_u32 v5, s18, v5
	v_add_u32_e32 v14, 0x6300, v77
	v_mad_u64_u32 v[10:11], s[18:19], s18, v3, 0
	v_add3_u32 v11, v11, v5, v4
	v_add_u32_e32 v3, 0x4200, v77
	v_add_u32_e32 v12, 0x4208, v77
	v_add_u32_e32 v16, 0x6308, v77
	v_lshl_add_u64 v[4:5], v[10:11], 1, s[10:11]
	ds_read2_b32 v[10:11], v3 offset1:1
	ds_read2_b32 v[12:13], v12 offset1:1
	ds_read2_b32 v[14:15], v14 offset1:1
	ds_read2_b32 v[16:17], v16 offset1:1
	v_lshl_add_u64 v[4:5], v[4:5], 0, s[16:17]
	v_lshl_add_u64 v[4:5], v[4:5], 0, v[66:67]
	s_waitcnt lgkmcnt(4)
	global_store_dwordx4 v[4:5], v[6:9], off nt
	s_waitcnt lgkmcnt(2)
	global_store_dwordx4 v[18:19], v[10:13], off offset:128 nt
	s_waitcnt lgkmcnt(0)
	global_store_dwordx4 v[4:5], v[14:17], off offset:128 nt

.LBB0_101:
	v_add_u32_e32 v9, 0x8400, v2
	ds_read2_b32 v[10:11], v9 offset1:1
	v_mov_b64_e32 v[12:13], s[20:21]
	v_mul_lo_u32 v9, s24, v8
	v_mad_u64_u32 v[14:15], s[10:11], s24, v6, v[12:13]
	v_add3_u32 v15, v7, v15, v9
	s_ashr_i32 s23, s22, 31
	v_lshl_add_u64 v[14:15], v[14:15], 0, s[22:23]
	v_add_u32_e32 v9, 0x9500, v2
	v_add_u32_e32 v18, 0xa600, v2
	v_lshl_add_u64 v[14:15], v[14:15], 0, v[68:69]
	v_add_u32_e32 v2, 0xb700, v2
	ds_read2_b32 v[16:17], v9 offset1:1
	ds_read2_b32 v[18:19], v18 offset1:1
	ds_read2_b32 v[20:21], v2 offset1:1
	s_waitcnt lgkmcnt(3)
	global_store_dwordx2 v[14:15], v[10:11], off nt
	v_mul_lo_u32 v2, s24, v5
	v_mad_u64_u32 v[10:11], s[10:11], s24, v3, v[12:13]
	v_add3_u32 v11, v4, v11, v2
	v_lshl_add_u64 v[10:11], v[10:11], 0, s[22:23]
	v_lshl_add_u64 v[10:11], v[10:11], 0, v[68:69]
	s_waitcnt lgkmcnt(2)
	global_store_dwordx2 v[10:11], v[16:17], off nt
	s_waitcnt lgkmcnt(1)
	global_store_dwordx2 v[14:15], v[18:19], off offset:64 nt
	s_waitcnt lgkmcnt(0)
	global_store_dwordx2 v[10:11], v[20:21], off offset:64 nt
	s_cbranch_execnz .LBB0_97
.LBB0_102:
	v_add_u32_e32 v2, 0x8400, v77
	v_add_u32_e32 v9, 0x8408, v77
	ds_read2_b32 v[10:11], v2 offset1:1
	ds_read2_b32 v[12:13], v9 offset1:1
	v_mul_lo_u32 v2, s24, v8
	v_mad_u64_u32 v[8:9], s[10:11], s24, v6, 0
	v_add3_u32 v9, v9, v2, v7
	s_ashr_i32 s23, s22, 31
	v_lshl_add_u64 v[6:7], v[8:9], 1, s[20:21]
	s_lshl_b64 s[10:11], s[22:23], 1
	v_lshl_add_u64 v[6:7], v[6:7], 0, s[10:11]
	v_add_u32_e32 v2, 0xa500, v77
	v_add_u32_e32 v8, 0xa508, v77
	v_lshl_add_u64 v[14:15], v[6:7], 0, v[66:67]
	ds_read2_b32 v[6:7], v2 offset1:1
	ds_read2_b32 v[8:9], v8 offset1:1
	v_mul_lo_u32 v5, s24, v5
	v_mad_u64_u32 v[2:3], s[16:17], s24, v3, 0
	v_add3_u32 v3, v3, v5, v4
	s_waitcnt lgkmcnt(2)
	global_store_dwordx4 v[14:15], v[10:13], off nt
	v_lshl_add_u64 v[16:17], v[2:3], 1, s[20:21]
	v_add_u32_e32 v2, 0xc600, v77
	v_add_u32_e32 v4, 0xc608, v77
	v_add_u32_e32 v10, 0xe700, v77
	v_add_u32_e32 v12, 0xe708, v77
	ds_read2_b32 v[2:3], v2 offset1:1
	ds_read2_b32 v[4:5], v4 offset1:1
	ds_read2_b32 v[10:11], v10 offset1:1
	ds_read2_b32 v[12:13], v12 offset1:1
	v_lshl_add_u64 v[16:17], v[16:17], 0, s[10:11]
	v_lshl_add_u64 v[16:17], v[16:17], 0, v[66:67]
	s_waitcnt lgkmcnt(4)
	global_store_dwordx4 v[16:17], v[6:9], off nt
	s_waitcnt lgkmcnt(2)
	global_store_dwordx4 v[14:15], v[2:5], off offset:128 nt
	s_waitcnt lgkmcnt(0)
	global_store_dwordx4 v[16:17], v[10:13], off offset:128 nt
	s_and_saveexec_b64 s[16:17], s[6:7]
	s_cbranch_execz .LBB0_59

.LBB0_360:
	s_waitcnt lgkmcnt(0)
	s_barrier
	s_waitcnt vmcnt(2)
	v_add_u32_e32 v3, s19, v70
	v_add_u32_e32 v5, s19, v72
	s_mov_b64 s[8:9], -1
	s_and_b64 vcc, exec, s[52:53]
	v_add_u32_e32 v4, v71, v66
	s_waitcnt vmcnt(0)
	v_ashrrev_i32_e32 v9, 31, v3
	v_mul_lo_u32 v8, s37, v3
	v_ashrrev_i32_e32 v7, 31, v5
	v_mul_lo_u32 v6, s37, v5
	s_cbranch_vccz .LBB0_362
	ds_read2_b32 v[10:11], v4 offset1:1
	v_mov_b64_e32 v[12:13], s[0:1]
	v_mul_lo_u32 v2, s36, v9
	v_mad_u64_u32 v[14:15], s[8:9], s36, v3, v[12:13]
	v_add3_u32 v15, v8, v15, v2
	s_ashr_i32 s27, s26, 31
	v_lshl_add_u64 v[14:15], v[14:15], 0, s[26:27]
	v_lshl_add_u64 v[14:15], v[14:15], 0, v[66:67]
	v_add_u32_e32 v2, 0x1100, v4
	s_waitcnt lgkmcnt(0)
	global_store_dwordx2 v[14:15], v[10:11], off nt
	ds_read2_b32 v[10:11], v2 offset1:1
	v_mul_lo_u32 v2, s36, v7
	v_mad_u64_u32 v[12:13], s[8:9], s36, v5, v[12:13]
	v_add3_u32 v13, v6, v13, v2
	v_lshl_add_u64 v[12:13], v[12:13], 0, s[26:27]
	v_lshl_add_u64 v[12:13], v[12:13], 0, v[66:67]
	v_add_u32_e32 v2, 0x2200, v4
	s_waitcnt lgkmcnt(0)
	global_store_dwordx2 v[12:13], v[10:11], off nt
	ds_read2_b32 v[10:11], v2 offset1:1
	v_add_u32_e32 v2, 0x3300, v4
	s_mov_b64 s[8:9], 0
	s_waitcnt lgkmcnt(0)
	global_store_dwordx2 v[14:15], v[10:11], off offset:64 nt
	ds_read2_b32 v[10:11], v2 offset1:1
	s_waitcnt lgkmcnt(0)
	global_store_dwordx2 v[12:13], v[10:11], off offset:64 nt
.LBB0_362:
	s_andn2_b64 vcc, exec, s[8:9]
	v_lshlrev_b32_e32 v2, 1, v68
	s_cbranch_vccnz .LBB0_364
	ds_read2_b32 v[10:11], v73 offset1:1
	ds_read2_b32 v[12:13], v73 offset0:2 offset1:3
	v_mul_lo_u32 v9, s36, v9
	v_mad_u64_u32 v[14:15], s[8:9], s36, v3, 0
	v_add3_u32 v15, v15, v9, v8
	s_ashr_i32 s27, s26, 31
	v_lshl_add_u64 v[8:9], v[14:15], 1, s[0:1]
	s_lshl_b64 s[8:9], s[26:27], 1
	v_lshl_add_u64 v[8:9], v[8:9], 0, s[8:9]
	v_mov_b32_e32 v3, v195
	v_lshl_add_u64 v[14:15], v[8:9], 0, v[2:3]
	s_waitcnt lgkmcnt(0)
	global_store_dwordx4 v[14:15], v[10:13], off nt
	v_add_u32_e32 v8, 0x2100, v73
	v_mul_lo_u32 v7, s36, v7
	v_add_u32_e32 v10, 0x2108, v73
	v_mad_u64_u32 v[12:13], s[24:25], s36, v5, 0
	ds_read2_b32 v[8:9], v8 offset1:1
	ds_read2_b32 v[10:11], v10 offset1:1
	v_add3_u32 v13, v13, v7, v6
	v_lshl_add_u64 v[6:7], v[12:13], 1, s[0:1]
	v_lshl_add_u64 v[6:7], v[6:7], 0, s[8:9]
	v_lshl_add_u64 v[12:13], v[6:7], 0, v[2:3]
	v_add_u32_e32 v3, 0x4200, v73
	ds_read2_b32 v[6:7], v3 offset1:1
	v_add_u32_e32 v3, 0x4208, v73
	s_waitcnt lgkmcnt(1)
	global_store_dwordx4 v[12:13], v[8:11], off nt
	ds_read2_b32 v[8:9], v3 offset1:1
	v_add_u32_e32 v3, 0x6300, v73
	s_waitcnt lgkmcnt(0)
	global_store_dwordx4 v[14:15], v[6:9], off offset:128 nt
	ds_read2_b32 v[6:7], v3 offset1:1
	v_add_u32_e32 v3, 0x6308, v73
	ds_read2_b32 v[8:9], v3 offset1:1
	s_waitcnt lgkmcnt(0)
	global_store_dwordx4 v[12:13], v[6:9], off offset:128 nt

.LBB0_370:
	v_add_u32_e32 v10, 0x8400, v4
	ds_read2_b32 v[10:11], v10 offset1:1
	v_mov_b64_e32 v[12:13], s[38:39]
	v_mul_lo_u32 v16, s46, v9
	v_mad_u64_u32 v[14:15], s[0:1], s46, v3, v[12:13]
	v_add3_u32 v15, v8, v15, v16
	s_ashr_i32 s45, s44, 31
	v_lshl_add_u64 v[14:15], v[14:15], 0, s[44:45]
	v_lshl_add_u64 v[14:15], v[14:15], 0, v[66:67]
	s_waitcnt lgkmcnt(0)
	global_store_dwordx2 v[14:15], v[10:11], off nt
	v_add_u32_e32 v10, 0x9500, v4
	ds_read2_b32 v[10:11], v10 offset1:1
	v_mul_lo_u32 v16, s46, v7
	v_mad_u64_u32 v[12:13], s[0:1], s46, v5, v[12:13]
	v_add3_u32 v13, v6, v13, v16
	v_lshl_add_u64 v[12:13], v[12:13], 0, s[44:45]
	v_lshl_add_u64 v[12:13], v[12:13], 0, v[66:67]
	s_waitcnt lgkmcnt(0)
	global_store_dwordx2 v[12:13], v[10:11], off nt
	v_add_u32_e32 v10, 0xa600, v4
	ds_read2_b32 v[10:11], v10 offset1:1
	v_add_u32_e32 v4, 0xb700, v4
	s_waitcnt lgkmcnt(0)
	global_store_dwordx2 v[14:15], v[10:11], off offset:64 nt
	ds_read2_b32 v[10:11], v4 offset1:1
	s_waitcnt lgkmcnt(0)
	global_store_dwordx2 v[12:13], v[10:11], off offset:64 nt
	s_cbranch_execnz .LBB0_366
.LBB0_371:
	v_add_u32_e32 v4, 0x8400, v73
	ds_read2_b32 v[10:11], v4 offset1:1
	v_add_u32_e32 v4, 0x8408, v73
	ds_read2_b32 v[12:13], v4 offset1:1
	v_mul_lo_u32 v4, s46, v9
	v_mad_u64_u32 v[14:15], s[0:1], s46, v3, 0
	v_add3_u32 v15, v15, v4, v8
	s_ashr_i32 s45, s44, 31
	v_lshl_add_u64 v[8:9], v[14:15], 1, s[38:39]
	s_lshl_b64 s[0:1], s[44:45], 1
	v_lshl_add_u64 v[8:9], v[8:9], 0, s[0:1]
	v_mov_b32_e32 v3, v195
	v_add_u32_e32 v4, 0xa500, v73
	v_lshl_add_u64 v[14:15], v[8:9], 0, v[2:3]
	ds_read2_b32 v[8:9], v4 offset1:1
	v_add_u32_e32 v4, 0xa508, v73
	s_waitcnt lgkmcnt(1)
	global_store_dwordx4 v[14:15], v[10:13], off nt
	ds_read2_b32 v[10:11], v4 offset1:1
	v_mul_lo_u32 v7, s46, v7
	v_mad_u64_u32 v[4:5], s[8:9], s46, v5, 0
	v_add3_u32 v5, v5, v7, v6
	v_lshl_add_u64 v[4:5], v[4:5], 1, s[38:39]
	v_lshl_add_u64 v[4:5], v[4:5], 0, s[0:1]
	v_lshl_add_u64 v[6:7], v[4:5], 0, v[2:3]
	v_add_u32_e32 v2, 0xc600, v73
	v_add_u32_e32 v4, 0xc608, v73
	ds_read2_b32 v[2:3], v2 offset1:1
	ds_read2_b32 v[4:5], v4 offset1:1
	s_waitcnt lgkmcnt(2)
	global_store_dwordx4 v[6:7], v[8:11], off nt
	s_waitcnt lgkmcnt(0)
	global_store_dwordx4 v[14:15], v[2:5], off offset:128 nt
	s_nop 1
	v_add_u32_e32 v2, 0xe700, v73
	v_add_u32_e32 v4, 0xe708, v73
	ds_read2_b32 v[2:3], v2 offset1:1
	ds_read2_b32 v[4:5], v4 offset1:1
	s_waitcnt lgkmcnt(0)
	global_store_dwordx4 v[6:7], v[2:5], off offset:128 nt
	s_and_saveexec_b64 s[0:1], s[40:41]
	s_cbranch_execz .LBB0_328

.Lfc_p3_st0_slot_done:
	s_or_b64 exec, exec, s[16:17]
	s_waitcnt lgkmcnt(0)
	s_barrier
	ds_read_b32 v12, v13 offset:0
	v_add_u32_e32 v176, 0x0, v17
	ds_read2_b32 v[178:179], v176 offset1:1
	v_add_u32_e32 v180, 0x1100, v17
	ds_read2_b32 v[182:183], v180 offset1:1
	v_add_u32_e32 v184, 0x2200, v17
	ds_read2_b32 v[186:187], v184 offset1:1
	v_add_u32_e32 v188, 0x3300, v17
	ds_read2_b32 v[190:191], v188 offset1:1
	s_waitcnt lgkmcnt(3)
	global_store_dwordx2 v[28:29], v[178:179], off nt
	s_waitcnt lgkmcnt(2)
	global_store_dwordx2 v[30:31], v[182:183], off nt
	s_waitcnt lgkmcnt(1)
	global_store_dwordx2 v[28:29], v[186:187], off offset:64 nt
	s_waitcnt lgkmcnt(0)
	global_store_dwordx2 v[30:31], v[190:191], off offset:64 nt
	v_add_u32_e32 v176, 0x4400, v17
	ds_read2_b32 v[178:179], v176 offset1:1
	v_add_u32_e32 v180, 0x5500, v17
	ds_read2_b32 v[182:183], v180 offset1:1
	v_add_u32_e32 v184, 0x6600, v17
	ds_read2_b32 v[186:187], v184 offset1:1
	v_add_u32_e32 v188, 0x7700, v17
	ds_read2_b32 v[190:191], v188 offset1:1
	s_waitcnt lgkmcnt(3)
	global_store_dwordx2 v[32:33], v[178:179], off nt
	s_waitcnt lgkmcnt(2)
	global_store_dwordx2 v[34:35], v[182:183], off nt
	s_waitcnt lgkmcnt(1)
	global_store_dwordx2 v[32:33], v[186:187], off offset:64 nt
	s_waitcnt lgkmcnt(0)
	global_store_dwordx2 v[34:35], v[190:191], off offset:64 nt
	s_waitcnt lgkmcnt(0)
	s_mov_b32 s14, s25
	v_readfirstlane_b32 s25, v12
	s_cmp_lt_i32 s14, 0
	s_cbranch_scc1 .Lfc_p3_exit
	s_cmp_lt_i32 s25, 0
	s_cbranch_scc1 .Lfc_p3_st1_nonext
	s_bitcmp1_b32 s25, 30
	s_cbranch_scc1 .Lfc_p3_st1_noclaim
	v_cmp_eq_u32_e32 vcc, 0, v0
	s_and_saveexec_b64 s[16:17], vcc
	s_cbranch_execz .Lfc_p3_st1_claimed
	global_atomic_add v10, v195, v7, s[58:59] sc0
	global_load_dword v11, v195, s[60:61] sc1

.Lfc_p3_st1_slot_done:
	s_or_b64 exec, exec, s[16:17]
	s_waitcnt lgkmcnt(0)
	s_barrier
	ds_read_b32 v12, v13 offset:4
	v_add_u32_e32 v176, 0x8800, v17
	ds_read2_b32 v[178:179], v176 offset1:1
	v_add_u32_e32 v180, 0x9900, v17
	ds_read2_b32 v[182:183], v180 offset1:1
	v_add_u32_e32 v184, 0xaa00, v17
	ds_read2_b32 v[186:187], v184 offset1:1
	v_add_u32_e32 v188, 0xbb00, v17
	ds_read2_b32 v[190:191], v188 offset1:1
	s_waitcnt lgkmcnt(3)
	global_store_dwordx2 v[36:37], v[178:179], off nt
	s_waitcnt lgkmcnt(2)
	global_store_dwordx2 v[38:39], v[182:183], off nt
	s_waitcnt lgkmcnt(1)
	global_store_dwordx2 v[36:37], v[186:187], off offset:64 nt
	s_waitcnt lgkmcnt(0)
	global_store_dwordx2 v[38:39], v[190:191], off offset:64 nt
	v_add_u32_e32 v176, 0xcc00, v17
	ds_read2_b32 v[178:179], v176 offset1:1
	v_add_u32_e32 v180, 0xdd00, v17
	ds_read2_b32 v[182:183], v180 offset1:1
	v_add_u32_e32 v184, 0xee00, v17
	ds_read2_b32 v[186:187], v184 offset1:1
	v_add_u32_e32 v188, 0xff00, v17
	ds_read2_b32 v[190:191], v188 offset1:1
	s_waitcnt lgkmcnt(3)
	global_store_dwordx2 v[40:41], v[178:179], off nt
	s_waitcnt lgkmcnt(2)
	global_store_dwordx2 v[42:43], v[182:183], off nt
	s_waitcnt lgkmcnt(1)
	global_store_dwordx2 v[40:41], v[186:187], off offset:64 nt
	s_waitcnt lgkmcnt(0)
	global_store_dwordx2 v[42:43], v[190:191], off offset:64 nt
	s_waitcnt lgkmcnt(0)
	s_mov_b32 s14, s25
	v_readfirstlane_b32 s25, v12
	s_cmp_lt_i32 s14, 0
	s_cbranch_scc1 .Lfc_p3_exit
	s_branch .Lfc_p3_top

.LBB0_526:
	s_waitcnt lgkmcnt(0)
	s_barrier
	s_waitcnt vmcnt(2)
	v_add_u32_e32 v3, s17, v70
	v_add_u32_e32 v5, s17, v72
	s_mov_b64 s[8:9], -1
	s_and_b64 vcc, exec, s[52:53]
	v_add_u32_e32 v4, v71, v66
	s_waitcnt vmcnt(0)
	v_ashrrev_i32_e32 v9, 31, v3
	v_mul_lo_u32 v8, s37, v3
	v_ashrrev_i32_e32 v7, 31, v5
	v_mul_lo_u32 v6, s37, v5
	s_cbranch_vccz .LBB0_528
	ds_read2_b32 v[10:11], v4 offset1:1
	v_mov_b64_e32 v[12:13], s[22:23]
	v_mul_lo_u32 v2, s36, v9
	v_mad_u64_u32 v[14:15], s[8:9], s36, v3, v[12:13]
	v_add3_u32 v15, v8, v15, v2
	s_ashr_i32 s29, s28, 31
	v_lshl_add_u64 v[14:15], v[14:15], 0, s[28:29]
	v_lshl_add_u64 v[14:15], v[14:15], 0, v[66:67]
	v_add_u32_e32 v2, 0x1100, v4
	s_waitcnt lgkmcnt(0)
	global_store_dwordx2 v[14:15], v[10:11], off nt
	ds_read2_b32 v[10:11], v2 offset1:1
	v_mul_lo_u32 v2, s36, v7
	v_mad_u64_u32 v[12:13], s[8:9], s36, v5, v[12:13]
	v_add3_u32 v13, v6, v13, v2
	v_lshl_add_u64 v[12:13], v[12:13], 0, s[28:29]
	v_lshl_add_u64 v[12:13], v[12:13], 0, v[66:67]
	v_add_u32_e32 v2, 0x2200, v4
	s_waitcnt lgkmcnt(0)
	global_store_dwordx2 v[12:13], v[10:11], off nt
	ds_read2_b32 v[10:11], v2 offset1:1
	v_add_u32_e32 v2, 0x3300, v4
	s_mov_b64 s[8:9], 0
	s_waitcnt lgkmcnt(0)
	global_store_dwordx2 v[14:15], v[10:11], off offset:64 nt
	ds_read2_b32 v[10:11], v2 offset1:1
	s_waitcnt lgkmcnt(0)
	global_store_dwordx2 v[12:13], v[10:11], off offset:64 nt
.LBB0_528:
	s_andn2_b64 vcc, exec, s[8:9]
	v_lshlrev_b32_e32 v2, 1, v68
	s_cbranch_vccnz .LBB0_530
	ds_read2_b32 v[10:11], v73 offset1:1
	ds_read2_b32 v[12:13], v73 offset0:2 offset1:3
	v_mul_lo_u32 v9, s36, v9
	v_mad_u64_u32 v[14:15], s[8:9], s36, v3, 0
	v_add3_u32 v15, v15, v9, v8
	s_ashr_i32 s29, s28, 31
	v_lshl_add_u64 v[8:9], v[14:15], 1, s[22:23]
	s_lshl_b64 s[8:9], s[28:29], 1
	v_lshl_add_u64 v[8:9], v[8:9], 0, s[8:9]
	v_mov_b32_e32 v3, v195
	v_lshl_add_u64 v[14:15], v[8:9], 0, v[2:3]
	s_waitcnt lgkmcnt(0)
	global_store_dwordx4 v[14:15], v[10:13], off nt
	v_add_u32_e32 v8, 0x2100, v73
	v_mul_lo_u32 v7, s36, v7
	v_add_u32_e32 v10, 0x2108, v73
	v_mad_u64_u32 v[12:13], s[18:19], s36, v5, 0
	ds_read2_b32 v[8:9], v8 offset1:1
	ds_read2_b32 v[10:11], v10 offset1:1
	v_add3_u32 v13, v13, v7, v6
	v_lshl_add_u64 v[6:7], v[12:13], 1, s[22:23]
	v_lshl_add_u64 v[6:7], v[6:7], 0, s[8:9]
	v_lshl_add_u64 v[12:13], v[6:7], 0, v[2:3]
	v_add_u32_e32 v3, 0x4200, v73
	ds_read2_b32 v[6:7], v3 offset1:1
	v_add_u32_e32 v3, 0x4208, v73
	s_waitcnt lgkmcnt(1)
	global_store_dwordx4 v[12:13], v[8:11], off nt
	ds_read2_b32 v[8:9], v3 offset1:1
	v_add_u32_e32 v3, 0x6300, v73
	s_waitcnt lgkmcnt(0)
	global_store_dwordx4 v[14:15], v[6:9], off offset:128 nt
	ds_read2_b32 v[6:7], v3 offset1:1
	v_add_u32_e32 v3, 0x6308, v73
	ds_read2_b32 v[8:9], v3 offset1:1
	s_waitcnt lgkmcnt(0)
	global_store_dwordx4 v[12:13], v[6:9], off offset:128 nt

.LBB0_536:
	v_add_u32_e32 v10, 0x8400, v4
	ds_read2_b32 v[10:11], v10 offset1:1
	v_mov_b64_e32 v[12:13], s[38:39]
	v_mul_lo_u32 v16, s46, v9
	v_mad_u64_u32 v[14:15], s[8:9], s46, v3, v[12:13]
	v_add3_u32 v15, v8, v15, v16
	s_ashr_i32 s45, s44, 31
	v_lshl_add_u64 v[14:15], v[14:15], 0, s[44:45]
	v_lshl_add_u64 v[14:15], v[14:15], 0, v[66:67]
	s_waitcnt lgkmcnt(0)
	global_store_dwordx2 v[14:15], v[10:11], off nt
	v_add_u32_e32 v10, 0x9500, v4
	ds_read2_b32 v[10:11], v10 offset1:1
	v_mul_lo_u32 v16, s46, v7
	v_mad_u64_u32 v[12:13], s[8:9], s46, v5, v[12:13]
	v_add3_u32 v13, v6, v13, v16
	v_lshl_add_u64 v[12:13], v[12:13], 0, s[44:45]
	v_lshl_add_u64 v[12:13], v[12:13], 0, v[66:67]
	s_waitcnt lgkmcnt(0)
	global_store_dwordx2 v[12:13], v[10:11], off nt
	v_add_u32_e32 v10, 0xa600, v4
	ds_read2_b32 v[10:11], v10 offset1:1
	v_add_u32_e32 v4, 0xb700, v4
	s_waitcnt lgkmcnt(0)
	global_store_dwordx2 v[14:15], v[10:11], off offset:64 nt
	ds_read2_b32 v[10:11], v4 offset1:1
	s_waitcnt lgkmcnt(0)
	global_store_dwordx2 v[12:13], v[10:11], off offset:64 nt
	s_cbranch_execnz .LBB0_532
.LBB0_537:
	v_add_u32_e32 v4, 0x8400, v73
	ds_read2_b32 v[10:11], v4 offset1:1
	v_add_u32_e32 v4, 0x8408, v73
	ds_read2_b32 v[12:13], v4 offset1:1
	v_mul_lo_u32 v4, s46, v9
	v_mad_u64_u32 v[14:15], s[8:9], s46, v3, 0
	v_add3_u32 v15, v15, v4, v8
	s_ashr_i32 s45, s44, 31
	v_lshl_add_u64 v[8:9], v[14:15], 1, s[38:39]
	s_lshl_b64 s[8:9], s[44:45], 1
	v_lshl_add_u64 v[8:9], v[8:9], 0, s[8:9]
	v_mov_b32_e32 v3, v195
	v_add_u32_e32 v4, 0xa500, v73
	v_lshl_add_u64 v[14:15], v[8:9], 0, v[2:3]
	ds_read2_b32 v[8:9], v4 offset1:1
	v_add_u32_e32 v4, 0xa508, v73
	s_waitcnt lgkmcnt(1)
	global_store_dwordx4 v[14:15], v[10:13], off nt
	ds_read2_b32 v[10:11], v4 offset1:1
	v_mul_lo_u32 v7, s46, v7
	v_mad_u64_u32 v[4:5], s[18:19], s46, v5, 0
	v_add3_u32 v5, v5, v7, v6
	v_lshl_add_u64 v[4:5], v[4:5], 1, s[38:39]
	v_lshl_add_u64 v[4:5], v[4:5], 0, s[8:9]
	v_lshl_add_u64 v[6:7], v[4:5], 0, v[2:3]
	v_add_u32_e32 v2, 0xc600, v73
	v_add_u32_e32 v4, 0xc608, v73
	ds_read2_b32 v[2:3], v2 offset1:1
	ds_read2_b32 v[4:5], v4 offset1:1
	s_waitcnt lgkmcnt(2)
	global_store_dwordx4 v[6:7], v[8:11], off nt
	s_waitcnt lgkmcnt(0)
	global_store_dwordx4 v[14:15], v[2:5], off offset:128 nt
	s_nop 1
	v_add_u32_e32 v2, 0xe700, v73
	v_add_u32_e32 v4, 0xe708, v73
	ds_read2_b32 v[2:3], v2 offset1:1
	ds_read2_b32 v[4:5], v4 offset1:1
	s_waitcnt lgkmcnt(0)
	global_store_dwordx4 v[6:7], v[2:5], off offset:128 nt
	s_and_saveexec_b64 s[8:9], s[40:41]
	s_cbranch_execz .LBB0_494

.LBB0_920:
	s_waitcnt lgkmcnt(0)
	s_barrier
	s_waitcnt vmcnt(2)
	v_add_u32_e32 v3, s29, v70
	v_add_u32_e32 v5, s29, v72
	s_mov_b64 s[8:9], -1
	s_and_b64 vcc, exec, s[56:57]
	v_add_u32_e32 v4, v71, v66
	s_waitcnt vmcnt(0)
	v_ashrrev_i32_e32 v9, 31, v3
	v_mul_lo_u32 v8, s37, v3
	v_ashrrev_i32_e32 v7, 31, v5
	v_mul_lo_u32 v6, s37, v5
	s_cbranch_vccz .LBB0_922
	ds_read2_b32 v[10:11], v4 offset1:1
	v_mov_b64_e32 v[12:13], s[26:27]
	v_mul_lo_u32 v2, s36, v9
	v_mad_u64_u32 v[14:15], s[8:9], s36, v3, v[12:13]
	v_add3_u32 v15, v8, v15, v2
	s_ashr_i32 s29, s28, 31
	v_lshl_add_u64 v[14:15], v[14:15], 0, s[28:29]
	v_lshl_add_u64 v[14:15], v[14:15], 0, v[66:67]
	v_add_u32_e32 v2, 0x1100, v4
	s_waitcnt lgkmcnt(0)
	global_store_dwordx2 v[14:15], v[10:11], off nt
	ds_read2_b32 v[10:11], v2 offset1:1
	v_mul_lo_u32 v2, s36, v7
	v_mad_u64_u32 v[12:13], s[8:9], s36, v5, v[12:13]
	v_add3_u32 v13, v6, v13, v2
	v_lshl_add_u64 v[12:13], v[12:13], 0, s[28:29]
	v_lshl_add_u64 v[12:13], v[12:13], 0, v[66:67]
	v_add_u32_e32 v2, 0x2200, v4
	s_waitcnt lgkmcnt(0)
	global_store_dwordx2 v[12:13], v[10:11], off nt
	ds_read2_b32 v[10:11], v2 offset1:1
	v_add_u32_e32 v2, 0x3300, v4
	s_mov_b64 s[8:9], 0
	s_waitcnt lgkmcnt(0)
	global_store_dwordx2 v[14:15], v[10:11], off offset:64 nt
	ds_read2_b32 v[10:11], v2 offset1:1
	s_waitcnt lgkmcnt(0)
	global_store_dwordx2 v[12:13], v[10:11], off offset:64 nt
.LBB0_922:
	s_andn2_b64 vcc, exec, s[8:9]
	v_lshlrev_b32_e32 v2, 1, v68
	s_cbranch_vccnz .LBB0_924
	ds_read2_b32 v[10:11], v73 offset1:1
	ds_read2_b32 v[12:13], v73 offset0:2 offset1:3
	v_mul_lo_u32 v9, s36, v9
	v_mad_u64_u32 v[14:15], s[8:9], s36, v3, 0
	v_add3_u32 v15, v15, v9, v8
	s_ashr_i32 s29, s28, 31
	v_lshl_add_u64 v[8:9], v[14:15], 1, s[26:27]
	s_lshl_b64 s[8:9], s[28:29], 1
	v_lshl_add_u64 v[8:9], v[8:9], 0, s[8:9]
	v_mov_b32_e32 v3, v195
	v_lshl_add_u64 v[14:15], v[8:9], 0, v[2:3]
	s_waitcnt lgkmcnt(0)
	global_store_dwordx4 v[14:15], v[10:13], off nt
	v_add_u32_e32 v8, 0x2100, v73
	v_mul_lo_u32 v7, s36, v7
	v_add_u32_e32 v10, 0x2108, v73
	v_mad_u64_u32 v[12:13], s[28:29], s36, v5, 0
	ds_read2_b32 v[8:9], v8 offset1:1
	ds_read2_b32 v[10:11], v10 offset1:1
	v_add3_u32 v13, v13, v7, v6
	v_lshl_add_u64 v[6:7], v[12:13], 1, s[26:27]
	v_lshl_add_u64 v[6:7], v[6:7], 0, s[8:9]
	v_lshl_add_u64 v[12:13], v[6:7], 0, v[2:3]
	v_add_u32_e32 v3, 0x4200, v73
	ds_read2_b32 v[6:7], v3 offset1:1
	v_add_u32_e32 v3, 0x4208, v73
	s_waitcnt lgkmcnt(1)
	global_store_dwordx4 v[12:13], v[8:11], off nt
	ds_read2_b32 v[8:9], v3 offset1:1
	v_add_u32_e32 v3, 0x6300, v73
	s_waitcnt lgkmcnt(0)
	global_store_dwordx4 v[14:15], v[6:9], off offset:128 nt
	ds_read2_b32 v[6:7], v3 offset1:1
	v_add_u32_e32 v3, 0x6308, v73
	ds_read2_b32 v[8:9], v3 offset1:1
	s_waitcnt lgkmcnt(0)
	global_store_dwordx4 v[12:13], v[6:9], off offset:128 nt

.LBB0_931:
	v_add_u32_e32 v4, 0x8400, v73
	ds_read2_b32 v[10:11], v4 offset1:1
	v_add_u32_e32 v4, 0x8408, v73
	ds_read2_b32 v[12:13], v4 offset1:1
	v_mul_lo_u32 v4, s46, v9
	v_mad_u64_u32 v[14:15], s[8:9], s46, v3, 0
	v_add3_u32 v15, v15, v4, v8
	s_ashr_i32 s45, s44, 31
	v_lshl_add_u64 v[8:9], v[14:15], 1, s[38:39]
	s_lshl_b64 s[8:9], s[44:45], 1
	v_lshl_add_u64 v[8:9], v[8:9], 0, s[8:9]
	v_mov_b32_e32 v3, v195
	v_add_u32_e32 v4, 0xa500, v73
	v_lshl_add_u64 v[14:15], v[8:9], 0, v[2:3]
	ds_read2_b32 v[8:9], v4 offset1:1
	v_add_u32_e32 v4, 0xa508, v73
	s_waitcnt lgkmcnt(1)
	global_store_dwordx4 v[14:15], v[10:13], off nt
	ds_read2_b32 v[10:11], v4 offset1:1
	v_mul_lo_u32 v7, s46, v7
	v_mad_u64_u32 v[4:5], s[26:27], s46, v5, 0
	v_add3_u32 v5, v5, v7, v6
	v_lshl_add_u64 v[4:5], v[4:5], 1, s[38:39]
	v_lshl_add_u64 v[4:5], v[4:5], 0, s[8:9]
	v_lshl_add_u64 v[6:7], v[4:5], 0, v[2:3]
	v_add_u32_e32 v2, 0xc600, v73
	v_add_u32_e32 v4, 0xc608, v73
	ds_read2_b32 v[2:3], v2 offset1:1
	ds_read2_b32 v[4:5], v4 offset1:1
	s_waitcnt lgkmcnt(2)
	global_store_dwordx4 v[6:7], v[8:11], off nt
	s_waitcnt lgkmcnt(0)
	global_store_dwordx4 v[14:15], v[2:5], off offset:128 nt
	s_nop 1
	v_add_u32_e32 v2, 0xe700, v73
	v_add_u32_e32 v4, 0xe708, v73
	ds_read2_b32 v[2:3], v2 offset1:1
	ds_read2_b32 v[4:5], v4 offset1:1
	s_waitcnt lgkmcnt(0)
	global_store_dwordx4 v[6:7], v[2:5], off offset:128 nt
	s_and_saveexec_b64 s[8:9], s[40:41]
	s_cbranch_execz .LBB0_888

.LBB0_1056:
	s_waitcnt lgkmcnt(0)
	s_barrier
	s_waitcnt vmcnt(2)
	v_add_u32_e32 v3, s19, v70
	v_add_u32_e32 v5, s19, v72
	s_mov_b64 s[8:9], -1
	s_and_b64 vcc, exec, s[60:61]
	v_add_u32_e32 v4, v71, v66
	s_waitcnt vmcnt(0)
	v_ashrrev_i32_e32 v9, 31, v3
	v_mul_lo_u32 v8, s29, v3
	v_ashrrev_i32_e32 v7, 31, v5
	v_mul_lo_u32 v6, s29, v5
	s_cbranch_vccz .LBB0_1058
	ds_read2_b32 v[10:11], v4 offset1:1
	v_mov_b64_e32 v[12:13], s[22:23]
	v_mul_lo_u32 v2, s28, v9
	v_mad_u64_u32 v[14:15], s[8:9], s28, v3, v[12:13]
	v_add3_u32 v15, v8, v15, v2
	s_ashr_i32 s27, s26, 31
	v_lshl_add_u64 v[14:15], v[14:15], 0, s[26:27]
	v_lshl_add_u64 v[14:15], v[14:15], 0, v[66:67]
	v_add_u32_e32 v2, 0x1100, v4
	s_waitcnt lgkmcnt(0)
	global_store_dwordx2 v[14:15], v[10:11], off nt
	ds_read2_b32 v[10:11], v2 offset1:1
	v_mul_lo_u32 v2, s28, v7
	v_mad_u64_u32 v[12:13], s[8:9], s28, v5, v[12:13]
	v_add3_u32 v13, v6, v13, v2
	v_lshl_add_u64 v[12:13], v[12:13], 0, s[26:27]
	v_lshl_add_u64 v[12:13], v[12:13], 0, v[66:67]
	v_add_u32_e32 v2, 0x2200, v4
	s_waitcnt lgkmcnt(0)
	global_store_dwordx2 v[12:13], v[10:11], off nt
	ds_read2_b32 v[10:11], v2 offset1:1
	v_add_u32_e32 v2, 0x3300, v4
	s_mov_b64 s[8:9], 0
	s_waitcnt lgkmcnt(0)
	global_store_dwordx2 v[14:15], v[10:11], off offset:64 nt
	ds_read2_b32 v[10:11], v2 offset1:1
	s_waitcnt lgkmcnt(0)
	global_store_dwordx2 v[12:13], v[10:11], off offset:64 nt
.LBB0_1058:
	s_andn2_b64 vcc, exec, s[8:9]
	v_lshlrev_b32_e32 v2, 1, v68
	s_cbranch_vccnz .LBB0_1060
	ds_read2_b32 v[10:11], v73 offset1:1
	ds_read2_b32 v[12:13], v73 offset0:2 offset1:3
	v_mul_lo_u32 v9, s28, v9
	v_mad_u64_u32 v[14:15], s[8:9], s28, v3, 0
	v_add3_u32 v15, v15, v9, v8
	s_ashr_i32 s27, s26, 31
	v_lshl_add_u64 v[8:9], v[14:15], 1, s[22:23]
	s_lshl_b64 s[8:9], s[26:27], 1
	v_lshl_add_u64 v[8:9], v[8:9], 0, s[8:9]
	v_mov_b32_e32 v3, v195
	v_lshl_add_u64 v[14:15], v[8:9], 0, v[2:3]
	s_waitcnt lgkmcnt(0)
	global_store_dwordx4 v[14:15], v[10:13], off nt
	v_add_u32_e32 v8, 0x2100, v73
	v_mul_lo_u32 v7, s28, v7
	v_add_u32_e32 v10, 0x2108, v73
	v_mad_u64_u32 v[12:13], s[24:25], s28, v5, 0
	ds_read2_b32 v[8:9], v8 offset1:1
	ds_read2_b32 v[10:11], v10 offset1:1
	v_add3_u32 v13, v13, v7, v6
	v_lshl_add_u64 v[6:7], v[12:13], 1, s[22:23]
	v_lshl_add_u64 v[6:7], v[6:7], 0, s[8:9]
	v_lshl_add_u64 v[12:13], v[6:7], 0, v[2:3]
	v_add_u32_e32 v3, 0x4200, v73
	ds_read2_b32 v[6:7], v3 offset1:1
	v_add_u32_e32 v3, 0x4208, v73
	s_waitcnt lgkmcnt(1)
	global_store_dwordx4 v[12:13], v[8:11], off nt
	ds_read2_b32 v[8:9], v3 offset1:1
	v_add_u32_e32 v3, 0x6300, v73
	s_waitcnt lgkmcnt(0)
	global_store_dwordx4 v[14:15], v[6:9], off offset:128 nt
	ds_read2_b32 v[6:7], v3 offset1:1
	v_add_u32_e32 v3, 0x6308, v73
	ds_read2_b32 v[8:9], v3 offset1:1
	s_waitcnt lgkmcnt(0)
	global_store_dwordx4 v[12:13], v[6:9], off offset:128 nt

.LBB0_1066:
	v_add_u32_e32 v10, 0x8400, v4
	ds_read2_b32 v[10:11], v10 offset1:1
	v_mov_b64_e32 v[12:13], s[36:37]
	v_mul_lo_u32 v16, s44, v9
	v_mad_u64_u32 v[14:15], s[8:9], s44, v3, v[12:13]
	v_add3_u32 v15, v8, v15, v16
	s_ashr_i32 s39, s38, 31
	v_lshl_add_u64 v[14:15], v[14:15], 0, s[38:39]
	v_lshl_add_u64 v[14:15], v[14:15], 0, v[66:67]
	s_waitcnt lgkmcnt(0)
	global_store_dwordx2 v[14:15], v[10:11], off nt
	v_add_u32_e32 v10, 0x9500, v4
	ds_read2_b32 v[10:11], v10 offset1:1
	v_mul_lo_u32 v16, s44, v7
	v_mad_u64_u32 v[12:13], s[8:9], s44, v5, v[12:13]
	v_add3_u32 v13, v6, v13, v16
	v_lshl_add_u64 v[12:13], v[12:13], 0, s[38:39]
	v_lshl_add_u64 v[12:13], v[12:13], 0, v[66:67]
	s_waitcnt lgkmcnt(0)
	global_store_dwordx2 v[12:13], v[10:11], off nt
	v_add_u32_e32 v10, 0xa600, v4
	ds_read2_b32 v[10:11], v10 offset1:1
	v_add_u32_e32 v4, 0xb700, v4
	s_waitcnt lgkmcnt(0)
	global_store_dwordx2 v[14:15], v[10:11], off offset:64 nt
	ds_read2_b32 v[10:11], v4 offset1:1
	s_waitcnt lgkmcnt(0)
	global_store_dwordx2 v[12:13], v[10:11], off offset:64 nt
	s_cbranch_execnz .LBB0_1062
.LBB0_1067:
	v_add_u32_e32 v4, 0x8400, v73
	ds_read2_b32 v[10:11], v4 offset1:1
	v_add_u32_e32 v4, 0x8408, v73
	ds_read2_b32 v[12:13], v4 offset1:1
	v_mul_lo_u32 v4, s44, v9
	v_mad_u64_u32 v[14:15], s[8:9], s44, v3, 0
	v_add3_u32 v15, v15, v4, v8
	s_ashr_i32 s39, s38, 31
	v_lshl_add_u64 v[8:9], v[14:15], 1, s[36:37]
	s_lshl_b64 s[8:9], s[38:39], 1
	v_lshl_add_u64 v[8:9], v[8:9], 0, s[8:9]
	v_mov_b32_e32 v3, v195
	v_add_u32_e32 v4, 0xa500, v73
	v_lshl_add_u64 v[14:15], v[8:9], 0, v[2:3]
	ds_read2_b32 v[8:9], v4 offset1:1
	v_add_u32_e32 v4, 0xa508, v73
	s_waitcnt lgkmcnt(1)
	global_store_dwordx4 v[14:15], v[10:13], off nt
	ds_read2_b32 v[10:11], v4 offset1:1
	v_mul_lo_u32 v7, s44, v7
	v_mad_u64_u32 v[4:5], s[22:23], s44, v5, 0
	v_add3_u32 v5, v5, v7, v6
	v_lshl_add_u64 v[4:5], v[4:5], 1, s[36:37]
	v_lshl_add_u64 v[4:5], v[4:5], 0, s[8:9]
	v_lshl_add_u64 v[6:7], v[4:5], 0, v[2:3]
	v_add_u32_e32 v2, 0xc600, v73
	v_add_u32_e32 v4, 0xc608, v73
	ds_read2_b32 v[2:3], v2 offset1:1
	ds_read2_b32 v[4:5], v4 offset1:1
	s_waitcnt lgkmcnt(2)
	global_store_dwordx4 v[6:7], v[8:11], off nt
	s_waitcnt lgkmcnt(0)
	global_store_dwordx4 v[14:15], v[2:5], off offset:128 nt
	s_nop 1
	v_add_u32_e32 v2, 0xe700, v73
	v_add_u32_e32 v4, 0xe708, v73
	ds_read2_b32 v[2:3], v2 offset1:1
	ds_read2_b32 v[4:5], v4 offset1:1
	s_waitcnt lgkmcnt(0)
	global_store_dwordx4 v[6:7], v[2:5], off offset:128 nt
	s_and_saveexec_b64 s[8:9], s[40:41]
	s_cbranch_execz .LBB0_1024

.LBB0_1111:
	s_waitcnt lgkmcnt(0)
	s_barrier
	s_waitcnt vmcnt(2)
	v_add_u32_e32 v3, s7, v70
	v_add_u32_e32 v5, s7, v72
	s_mov_b64 s[8:9], -1
	s_and_b64 vcc, exec, s[56:57]
	v_add_u32_e32 v4, v71, v66
	s_waitcnt vmcnt(0)
	v_ashrrev_i32_e32 v9, 31, v3
	v_mul_lo_u32 v8, s23, v3
	v_ashrrev_i32_e32 v7, 31, v5
	v_mul_lo_u32 v6, s23, v5
	s_cbranch_vccz .LBB0_1113
	ds_read2_b32 v[10:11], v4 offset1:1
	v_mov_b64_e32 v[12:13], s[0:1]
	v_mul_lo_u32 v2, s22, v9
	v_mad_u64_u32 v[14:15], s[8:9], s22, v3, v[12:13]
	v_add3_u32 v15, v8, v15, v2
	s_ashr_i32 s7, s6, 31
	v_lshl_add_u64 v[14:15], v[14:15], 0, s[6:7]
	v_lshl_add_u64 v[14:15], v[14:15], 0, v[66:67]
	v_add_u32_e32 v2, 0x1100, v4
	s_waitcnt lgkmcnt(0)
	global_store_dwordx2 v[14:15], v[10:11], off nt
	ds_read2_b32 v[10:11], v2 offset1:1
	v_mul_lo_u32 v2, s22, v7
	v_mad_u64_u32 v[12:13], s[8:9], s22, v5, v[12:13]
	v_add3_u32 v13, v6, v13, v2
	v_lshl_add_u64 v[12:13], v[12:13], 0, s[6:7]
	v_lshl_add_u64 v[12:13], v[12:13], 0, v[66:67]
	v_add_u32_e32 v2, 0x2200, v4
	s_waitcnt lgkmcnt(0)
	global_store_dwordx2 v[12:13], v[10:11], off nt
	ds_read2_b32 v[10:11], v2 offset1:1
	v_add_u32_e32 v2, 0x3300, v4
	s_mov_b64 s[8:9], 0
	s_waitcnt lgkmcnt(0)
	global_store_dwordx2 v[14:15], v[10:11], off offset:64 nt
	ds_read2_b32 v[10:11], v2 offset1:1
	s_waitcnt lgkmcnt(0)
	global_store_dwordx2 v[12:13], v[10:11], off offset:64 nt
.LBB0_1113:
	s_andn2_b64 vcc, exec, s[8:9]
	v_lshlrev_b32_e32 v2, 1, v68
	s_cbranch_vccnz .LBB0_1115
	ds_read2_b32 v[10:11], v73 offset1:1
	ds_read2_b32 v[12:13], v73 offset0:2 offset1:3
	v_mul_lo_u32 v9, s22, v9
	v_mad_u64_u32 v[14:15], s[8:9], s22, v3, 0
	v_add3_u32 v15, v15, v9, v8
	s_ashr_i32 s7, s6, 31
	v_lshl_add_u64 v[8:9], v[14:15], 1, s[0:1]
	s_lshl_b64 s[6:7], s[6:7], 1
	v_lshl_add_u64 v[8:9], v[8:9], 0, s[6:7]
	v_mov_b32_e32 v3, v195
	v_lshl_add_u64 v[14:15], v[8:9], 0, v[2:3]
	s_waitcnt lgkmcnt(0)
	global_store_dwordx4 v[14:15], v[10:13], off nt
	v_add_u32_e32 v8, 0x2100, v73
	v_mul_lo_u32 v7, s22, v7
	v_add_u32_e32 v10, 0x2108, v73
	v_mad_u64_u32 v[12:13], s[8:9], s22, v5, 0
	ds_read2_b32 v[8:9], v8 offset1:1
	ds_read2_b32 v[10:11], v10 offset1:1
	v_add3_u32 v13, v13, v7, v6
	v_lshl_add_u64 v[6:7], v[12:13], 1, s[0:1]
	v_lshl_add_u64 v[6:7], v[6:7], 0, s[6:7]
	v_lshl_add_u64 v[12:13], v[6:7], 0, v[2:3]
	v_add_u32_e32 v3, 0x4200, v73
	ds_read2_b32 v[6:7], v3 offset1:1
	v_add_u32_e32 v3, 0x4208, v73
	s_waitcnt lgkmcnt(1)
	global_store_dwordx4 v[12:13], v[8:11], off nt
	ds_read2_b32 v[8:9], v3 offset1:1
	v_add_u32_e32 v3, 0x6300, v73
	s_waitcnt lgkmcnt(0)
	global_store_dwordx4 v[14:15], v[6:9], off offset:128 nt
	ds_read2_b32 v[6:7], v3 offset1:1
	v_add_u32_e32 v3, 0x6308, v73
	ds_read2_b32 v[8:9], v3 offset1:1
	s_waitcnt lgkmcnt(0)
	global_store_dwordx4 v[12:13], v[6:9], off offset:128 nt

.LBB0_1121:
	v_add_u32_e32 v10, 0x8400, v4
	ds_read2_b32 v[10:11], v10 offset1:1
	v_mov_b64_e32 v[12:13], s[26:27]
	v_mul_lo_u32 v16, s36, v9
	v_mad_u64_u32 v[14:15], s[0:1], s36, v3, v[12:13]
	v_add3_u32 v15, v8, v15, v16
	s_ashr_i32 s29, s28, 31
	v_lshl_add_u64 v[14:15], v[14:15], 0, s[28:29]
	v_lshl_add_u64 v[14:15], v[14:15], 0, v[66:67]
	s_waitcnt lgkmcnt(0)
	global_store_dwordx2 v[14:15], v[10:11], off nt
	v_add_u32_e32 v10, 0x9500, v4
	ds_read2_b32 v[10:11], v10 offset1:1
	v_mul_lo_u32 v16, s36, v7
	v_mad_u64_u32 v[12:13], s[0:1], s36, v5, v[12:13]
	v_add3_u32 v13, v6, v13, v16
	v_lshl_add_u64 v[12:13], v[12:13], 0, s[28:29]
	v_lshl_add_u64 v[12:13], v[12:13], 0, v[66:67]
	s_waitcnt lgkmcnt(0)
	global_store_dwordx2 v[12:13], v[10:11], off nt
	v_add_u32_e32 v10, 0xa600, v4
	ds_read2_b32 v[10:11], v10 offset1:1
	v_add_u32_e32 v4, 0xb700, v4
	s_waitcnt lgkmcnt(0)
	global_store_dwordx2 v[14:15], v[10:11], off offset:64 nt
	ds_read2_b32 v[10:11], v4 offset1:1
	s_waitcnt lgkmcnt(0)
	global_store_dwordx2 v[12:13], v[10:11], off offset:64 nt
	s_cbranch_execnz .LBB0_1117
.LBB0_1122:
	v_add_u32_e32 v4, 0x8400, v73
	ds_read2_b32 v[10:11], v4 offset1:1
	v_add_u32_e32 v4, 0x8408, v73
	ds_read2_b32 v[12:13], v4 offset1:1
	v_mul_lo_u32 v4, s36, v9
	v_mad_u64_u32 v[14:15], s[0:1], s36, v3, 0
	v_add3_u32 v15, v15, v4, v8
	s_ashr_i32 s29, s28, 31
	v_lshl_add_u64 v[8:9], v[14:15], 1, s[26:27]
	s_lshl_b64 s[0:1], s[28:29], 1
	v_lshl_add_u64 v[8:9], v[8:9], 0, s[0:1]
	v_mov_b32_e32 v3, v195
	v_add_u32_e32 v4, 0xa500, v73
	v_lshl_add_u64 v[14:15], v[8:9], 0, v[2:3]
	ds_read2_b32 v[8:9], v4 offset1:1
	v_add_u32_e32 v4, 0xa508, v73
	s_waitcnt lgkmcnt(1)
	global_store_dwordx4 v[14:15], v[10:13], off nt
	ds_read2_b32 v[10:11], v4 offset1:1
	v_mul_lo_u32 v7, s36, v7
	v_mad_u64_u32 v[4:5], s[6:7], s36, v5, 0
	v_add3_u32 v5, v5, v7, v6
	v_lshl_add_u64 v[4:5], v[4:5], 1, s[26:27]
	v_lshl_add_u64 v[4:5], v[4:5], 0, s[0:1]
	v_lshl_add_u64 v[6:7], v[4:5], 0, v[2:3]
	v_add_u32_e32 v2, 0xc600, v73
	v_add_u32_e32 v4, 0xc608, v73
	ds_read2_b32 v[2:3], v2 offset1:1
	ds_read2_b32 v[4:5], v4 offset1:1
	s_waitcnt lgkmcnt(2)
	global_store_dwordx4 v[6:7], v[8:11], off nt
	s_waitcnt lgkmcnt(0)
	global_store_dwordx4 v[14:15], v[2:5], off offset:128 nt
	s_nop 1
	v_add_u32_e32 v2, 0xe700, v73
	v_add_u32_e32 v4, 0xe708, v73
	ds_read2_b32 v[2:3], v2 offset1:1
	ds_read2_b32 v[4:5], v4 offset1:1
	s_waitcnt lgkmcnt(0)
	global_store_dwordx4 v[6:7], v[2:5], off offset:128 nt
	s_and_saveexec_b64 s[0:1], s[40:41]
	s_cbranch_execz .LBB0_1079

.LBB0_1242:
	s_waitcnt lgkmcnt(0)
	s_barrier
	s_waitcnt vmcnt(2)
	v_add_u32_e32 v3, s19, v70
	v_add_u32_e32 v5, s19, v72
	s_mov_b64 s[8:9], -1
	s_and_b64 vcc, exec, s[60:61]
	v_add_u32_e32 v4, v71, v66
	s_waitcnt vmcnt(0)
	v_ashrrev_i32_e32 v9, 31, v3
	v_mul_lo_u32 v8, s39, v3
	v_ashrrev_i32_e32 v7, 31, v5
	v_mul_lo_u32 v6, s39, v5
	s_cbranch_vccz .LBB0_1244
	ds_read2_b32 v[10:11], v4 offset1:1
	v_mov_b64_e32 v[12:13], s[26:27]
	v_mul_lo_u32 v2, s38, v9
	v_mad_u64_u32 v[14:15], s[8:9], s38, v3, v[12:13]
	v_add3_u32 v15, v8, v15, v2
	s_ashr_i32 s37, s36, 31
	v_lshl_add_u64 v[14:15], v[14:15], 0, s[36:37]
	v_lshl_add_u64 v[14:15], v[14:15], 0, v[66:67]
	v_add_u32_e32 v2, 0x1100, v4
	s_waitcnt lgkmcnt(0)
	global_store_dwordx2 v[14:15], v[10:11], off nt
	ds_read2_b32 v[10:11], v2 offset1:1
	v_mul_lo_u32 v2, s38, v7
	v_mad_u64_u32 v[12:13], s[8:9], s38, v5, v[12:13]
	v_add3_u32 v13, v6, v13, v2
	v_lshl_add_u64 v[12:13], v[12:13], 0, s[36:37]
	v_lshl_add_u64 v[12:13], v[12:13], 0, v[66:67]
	v_add_u32_e32 v2, 0x2200, v4
	s_waitcnt lgkmcnt(0)
	global_store_dwordx2 v[12:13], v[10:11], off nt
	ds_read2_b32 v[10:11], v2 offset1:1
	v_add_u32_e32 v2, 0x3300, v4
	s_mov_b64 s[8:9], 0
	s_waitcnt lgkmcnt(0)
	global_store_dwordx2 v[14:15], v[10:11], off offset:64 nt
	ds_read2_b32 v[10:11], v2 offset1:1
	s_waitcnt lgkmcnt(0)
	global_store_dwordx2 v[12:13], v[10:11], off offset:64 nt
.LBB0_1244:
	s_andn2_b64 vcc, exec, s[8:9]
	v_lshlrev_b32_e32 v2, 1, v68
	s_cbranch_vccnz .LBB0_1246
	ds_read2_b32 v[10:11], v73 offset1:1
	ds_read2_b32 v[12:13], v73 offset0:2 offset1:3
	v_mul_lo_u32 v9, s38, v9
	v_mad_u64_u32 v[14:15], s[8:9], s38, v3, 0
	v_add3_u32 v15, v15, v9, v8
	s_ashr_i32 s37, s36, 31
	v_lshl_add_u64 v[8:9], v[14:15], 1, s[26:27]
	s_lshl_b64 s[8:9], s[36:37], 1
	v_lshl_add_u64 v[8:9], v[8:9], 0, s[8:9]
	v_mov_b32_e32 v3, v195
	v_lshl_add_u64 v[14:15], v[8:9], 0, v[2:3]
	s_waitcnt lgkmcnt(0)
	global_store_dwordx4 v[14:15], v[10:13], off nt
	v_add_u32_e32 v8, 0x2100, v73
	v_mul_lo_u32 v7, s38, v7
	v_add_u32_e32 v10, 0x2108, v73
	v_mad_u64_u32 v[12:13], s[24:25], s38, v5, 0
	ds_read2_b32 v[8:9], v8 offset1:1
	ds_read2_b32 v[10:11], v10 offset1:1
	v_add3_u32 v13, v13, v7, v6
	v_lshl_add_u64 v[6:7], v[12:13], 1, s[26:27]
	v_lshl_add_u64 v[6:7], v[6:7], 0, s[8:9]
	v_lshl_add_u64 v[12:13], v[6:7], 0, v[2:3]
	v_add_u32_e32 v3, 0x4200, v73
	ds_read2_b32 v[6:7], v3 offset1:1
	v_add_u32_e32 v3, 0x4208, v73
	s_waitcnt lgkmcnt(1)
	global_store_dwordx4 v[12:13], v[8:11], off nt
	ds_read2_b32 v[8:9], v3 offset1:1
	v_add_u32_e32 v3, 0x6300, v73
	s_waitcnt lgkmcnt(0)
	global_store_dwordx4 v[14:15], v[6:9], off offset:128 nt
	ds_read2_b32 v[6:7], v3 offset1:1
	v_add_u32_e32 v3, 0x6308, v73
	ds_read2_b32 v[8:9], v3 offset1:1
	s_waitcnt lgkmcnt(0)
	global_store_dwordx4 v[12:13], v[6:9], off offset:128 nt

.LBB0_1252:
	v_add_u32_e32 v10, 0x8400, v4
	ds_read2_b32 v[10:11], v10 offset1:1
	v_mov_b64_e32 v[12:13], s[44:45]
	v_mul_lo_u32 v16, s54, v9
	v_mad_u64_u32 v[14:15], s[8:9], s54, v3, v[12:13]
	v_add3_u32 v15, v8, v15, v16
	s_ashr_i32 s53, s52, 31
	v_lshl_add_u64 v[14:15], v[14:15], 0, s[52:53]
	v_lshl_add_u64 v[14:15], v[14:15], 0, v[66:67]
	s_waitcnt lgkmcnt(0)
	global_store_dwordx2 v[14:15], v[10:11], off nt
	v_add_u32_e32 v10, 0x9500, v4
	ds_read2_b32 v[10:11], v10 offset1:1
	v_mul_lo_u32 v16, s54, v7
	v_mad_u64_u32 v[12:13], s[8:9], s54, v5, v[12:13]
	v_add3_u32 v13, v6, v13, v16
	v_lshl_add_u64 v[12:13], v[12:13], 0, s[52:53]
	v_lshl_add_u64 v[12:13], v[12:13], 0, v[66:67]
	s_waitcnt lgkmcnt(0)
	global_store_dwordx2 v[12:13], v[10:11], off nt
	v_add_u32_e32 v10, 0xa600, v4
	ds_read2_b32 v[10:11], v10 offset1:1
	v_add_u32_e32 v4, 0xb700, v4
	s_waitcnt lgkmcnt(0)
	global_store_dwordx2 v[14:15], v[10:11], off offset:64 nt
	ds_read2_b32 v[10:11], v4 offset1:1
	s_waitcnt lgkmcnt(0)
	global_store_dwordx2 v[12:13], v[10:11], off offset:64 nt
	s_cbranch_execnz .LBB0_1248
.LBB0_1253:
	v_add_u32_e32 v4, 0x8400, v73
	ds_read2_b32 v[10:11], v4 offset1:1
	v_add_u32_e32 v4, 0x8408, v73
	ds_read2_b32 v[12:13], v4 offset1:1
	v_mul_lo_u32 v4, s54, v9
	v_mad_u64_u32 v[14:15], s[8:9], s54, v3, 0
	v_add3_u32 v15, v15, v4, v8
	s_ashr_i32 s53, s52, 31
	v_lshl_add_u64 v[8:9], v[14:15], 1, s[44:45]
	s_lshl_b64 s[8:9], s[52:53], 1
	v_lshl_add_u64 v[8:9], v[8:9], 0, s[8:9]
	v_mov_b32_e32 v3, v195
	v_add_u32_e32 v4, 0xa500, v73
	v_lshl_add_u64 v[14:15], v[8:9], 0, v[2:3]
	ds_read2_b32 v[8:9], v4 offset1:1
	v_add_u32_e32 v4, 0xa508, v73
	s_waitcnt lgkmcnt(1)
	global_store_dwordx4 v[14:15], v[10:13], off nt
	ds_read2_b32 v[10:11], v4 offset1:1
	v_mul_lo_u32 v7, s54, v7
	v_mad_u64_u32 v[4:5], s[24:25], s54, v5, 0
	v_add3_u32 v5, v5, v7, v6
	v_lshl_add_u64 v[4:5], v[4:5], 1, s[44:45]
	v_lshl_add_u64 v[4:5], v[4:5], 0, s[8:9]
	v_lshl_add_u64 v[6:7], v[4:5], 0, v[2:3]
	v_add_u32_e32 v2, 0xc600, v73
	v_add_u32_e32 v4, 0xc608, v73
	ds_read2_b32 v[2:3], v2 offset1:1
	ds_read2_b32 v[4:5], v4 offset1:1
	s_waitcnt lgkmcnt(2)
	global_store_dwordx4 v[6:7], v[8:11], off nt
	s_waitcnt lgkmcnt(0)
	global_store_dwordx4 v[14:15], v[2:5], off offset:128 nt
	s_nop 1
	v_add_u32_e32 v2, 0xe700, v73
	v_add_u32_e32 v4, 0xe708, v73
	ds_read2_b32 v[2:3], v2 offset1:1
	ds_read2_b32 v[4:5], v4 offset1:1
	s_waitcnt lgkmcnt(0)
	global_store_dwordx4 v[6:7], v[2:5], off offset:128 nt
	s_and_saveexec_b64 s[8:9], s[40:41]
	s_cbranch_execz .LBB0_1210

.LBB0_1298:
	s_waitcnt lgkmcnt(0)
	s_barrier
	s_waitcnt vmcnt(2)
	v_add_u32_e32 v3, s24, v70
	v_add_u32_e32 v5, s24, v72
	s_mov_b64 s[8:9], -1
	s_and_b64 vcc, exec, s[56:57]
	v_add_u32_e32 v4, v71, v66
	s_waitcnt vmcnt(0)
	v_ashrrev_i32_e32 v9, 31, v3
	v_mul_lo_u32 v8, s29, v3
	v_ashrrev_i32_e32 v7, 31, v5
	v_mul_lo_u32 v6, s29, v5
	s_cbranch_vccz .LBB0_1300
	ds_read2_b32 v[10:11], v4 offset1:1
	v_mov_b64_e32 v[12:13], s[6:7]
	v_mul_lo_u32 v2, s28, v9
	v_mad_u64_u32 v[14:15], s[8:9], s28, v3, v[12:13]
	v_add3_u32 v15, v8, v15, v2
	s_ashr_i32 s27, s26, 31
	v_lshl_add_u64 v[14:15], v[14:15], 0, s[26:27]
	v_lshl_add_u64 v[14:15], v[14:15], 0, v[66:67]
	v_add_u32_e32 v2, 0x1100, v4
	s_waitcnt lgkmcnt(0)
	global_store_dwordx2 v[14:15], v[10:11], off nt
	ds_read2_b32 v[10:11], v2 offset1:1
	v_mul_lo_u32 v2, s28, v7
	v_mad_u64_u32 v[12:13], s[8:9], s28, v5, v[12:13]
	v_add3_u32 v13, v6, v13, v2
	v_lshl_add_u64 v[12:13], v[12:13], 0, s[26:27]
	v_lshl_add_u64 v[12:13], v[12:13], 0, v[66:67]
	v_add_u32_e32 v2, 0x2200, v4
	s_waitcnt lgkmcnt(0)
	global_store_dwordx2 v[12:13], v[10:11], off nt
	ds_read2_b32 v[10:11], v2 offset1:1
	v_add_u32_e32 v2, 0x3300, v4
	s_mov_b64 s[8:9], 0
	s_waitcnt lgkmcnt(0)
	global_store_dwordx2 v[14:15], v[10:11], off offset:64 nt
	ds_read2_b32 v[10:11], v2 offset1:1
	s_waitcnt lgkmcnt(0)
	global_store_dwordx2 v[12:13], v[10:11], off offset:64 nt
.LBB0_1300:
	s_andn2_b64 vcc, exec, s[8:9]
	v_lshlrev_b32_e32 v2, 1, v68
	s_cbranch_vccnz .LBB0_1302
	ds_read2_b32 v[10:11], v73 offset1:1
	ds_read2_b32 v[12:13], v73 offset0:2 offset1:3
	v_mul_lo_u32 v9, s28, v9
	v_mad_u64_u32 v[14:15], s[8:9], s28, v3, 0
	v_add3_u32 v15, v15, v9, v8
	s_ashr_i32 s27, s26, 31
	v_lshl_add_u64 v[8:9], v[14:15], 1, s[6:7]
	s_lshl_b64 s[8:9], s[26:27], 1
	v_lshl_add_u64 v[8:9], v[8:9], 0, s[8:9]
	v_mov_b32_e32 v3, v195
	v_lshl_add_u64 v[14:15], v[8:9], 0, v[2:3]
	s_waitcnt lgkmcnt(0)
	global_store_dwordx4 v[14:15], v[10:13], off nt
	v_add_u32_e32 v8, 0x2100, v73
	v_mul_lo_u32 v7, s28, v7
	v_add_u32_e32 v10, 0x2108, v73
	v_mad_u64_u32 v[12:13], s[24:25], s28, v5, 0
	ds_read2_b32 v[8:9], v8 offset1:1
	ds_read2_b32 v[10:11], v10 offset1:1
	v_add3_u32 v13, v13, v7, v6
	v_lshl_add_u64 v[6:7], v[12:13], 1, s[6:7]
	v_lshl_add_u64 v[6:7], v[6:7], 0, s[8:9]
	v_lshl_add_u64 v[12:13], v[6:7], 0, v[2:3]
	v_add_u32_e32 v3, 0x4200, v73
	ds_read2_b32 v[6:7], v3 offset1:1
	v_add_u32_e32 v3, 0x4208, v73
	s_waitcnt lgkmcnt(1)
	global_store_dwordx4 v[12:13], v[8:11], off nt
	ds_read2_b32 v[8:9], v3 offset1:1
	v_add_u32_e32 v3, 0x6300, v73
	s_waitcnt lgkmcnt(0)
	global_store_dwordx4 v[14:15], v[6:9], off offset:128 nt
	ds_read2_b32 v[6:7], v3 offset1:1
	v_add_u32_e32 v3, 0x6308, v73
	ds_read2_b32 v[8:9], v3 offset1:1
	s_waitcnt lgkmcnt(0)
	global_store_dwordx4 v[12:13], v[6:9], off offset:128 nt

.LBB0_1308:
	v_add_u32_e32 v10, 0x8400, v4
	ds_read2_b32 v[10:11], v10 offset1:1
	v_mov_b64_e32 v[12:13], s[36:37]
	v_mul_lo_u32 v16, s44, v9
	v_mad_u64_u32 v[14:15], s[6:7], s44, v3, v[12:13]
	v_add3_u32 v15, v8, v15, v16
	s_ashr_i32 s39, s38, 31
	v_lshl_add_u64 v[14:15], v[14:15], 0, s[38:39]
	v_lshl_add_u64 v[14:15], v[14:15], 0, v[66:67]
	s_waitcnt lgkmcnt(0)
	global_store_dwordx2 v[14:15], v[10:11], off nt
	v_add_u32_e32 v10, 0x9500, v4
	ds_read2_b32 v[10:11], v10 offset1:1
	v_mul_lo_u32 v16, s44, v7
	v_mad_u64_u32 v[12:13], s[6:7], s44, v5, v[12:13]
	v_add3_u32 v13, v6, v13, v16
	v_lshl_add_u64 v[12:13], v[12:13], 0, s[38:39]
	v_lshl_add_u64 v[12:13], v[12:13], 0, v[66:67]
	s_waitcnt lgkmcnt(0)
	global_store_dwordx2 v[12:13], v[10:11], off nt
	v_add_u32_e32 v10, 0xa600, v4
	ds_read2_b32 v[10:11], v10 offset1:1
	v_add_u32_e32 v4, 0xb700, v4
	s_waitcnt lgkmcnt(0)
	global_store_dwordx2 v[14:15], v[10:11], off offset:64 nt
	ds_read2_b32 v[10:11], v4 offset1:1
	s_waitcnt lgkmcnt(0)
	global_store_dwordx2 v[12:13], v[10:11], off offset:64 nt
	s_cbranch_execnz .LBB0_1304
.LBB0_1309:
	v_add_u32_e32 v4, 0x8400, v73
	ds_read2_b32 v[10:11], v4 offset1:1
	v_add_u32_e32 v4, 0x8408, v73
	ds_read2_b32 v[12:13], v4 offset1:1
	v_mul_lo_u32 v4, s44, v9
	v_mad_u64_u32 v[14:15], s[6:7], s44, v3, 0
	v_add3_u32 v15, v15, v4, v8
	s_ashr_i32 s39, s38, 31
	v_lshl_add_u64 v[8:9], v[14:15], 1, s[36:37]
	s_lshl_b64 s[6:7], s[38:39], 1
	v_lshl_add_u64 v[8:9], v[8:9], 0, s[6:7]
	v_mov_b32_e32 v3, v195
	v_add_u32_e32 v4, 0xa500, v73
	v_lshl_add_u64 v[14:15], v[8:9], 0, v[2:3]
	ds_read2_b32 v[8:9], v4 offset1:1
	v_add_u32_e32 v4, 0xa508, v73
	s_waitcnt lgkmcnt(1)
	global_store_dwordx4 v[14:15], v[10:13], off nt
	ds_read2_b32 v[10:11], v4 offset1:1
	v_mul_lo_u32 v7, s44, v7
	v_mad_u64_u32 v[4:5], s[8:9], s44, v5, 0
	v_add3_u32 v5, v5, v7, v6
	v_lshl_add_u64 v[4:5], v[4:5], 1, s[36:37]
	v_lshl_add_u64 v[4:5], v[4:5], 0, s[6:7]
	v_lshl_add_u64 v[6:7], v[4:5], 0, v[2:3]
	v_add_u32_e32 v2, 0xc600, v73
	v_add_u32_e32 v4, 0xc608, v73
	ds_read2_b32 v[2:3], v2 offset1:1
	ds_read2_b32 v[4:5], v4 offset1:1
	s_waitcnt lgkmcnt(2)
	global_store_dwordx4 v[6:7], v[8:11], off nt
	s_waitcnt lgkmcnt(0)
	global_store_dwordx4 v[14:15], v[2:5], off offset:128 nt
	s_nop 1
	v_add_u32_e32 v2, 0xe700, v73
	v_add_u32_e32 v4, 0xe708, v73
	ds_read2_b32 v[2:3], v2 offset1:1
	ds_read2_b32 v[4:5], v4 offset1:1
	s_waitcnt lgkmcnt(0)
	global_store_dwordx4 v[6:7], v[2:5], off offset:128 nt
	s_and_saveexec_b64 s[6:7], s[40:41]
	s_cbranch_execz .LBB0_1266
